# speedup vs baseline: 1.0007x; 1.0007x over previous
_Z14combine_kernelPKfPKiS0_Pf:
	s_load_dwordx8 s[4:11], s[0:1], 0x0
	v_lshl_or_b32 v0, s2, 8, v0
	s_mov_b32 s0, 0x2aaaaaab
	v_mul_hi_i32 v1, v0, s0
	v_lshrrev_b32_e32 v2, 31, v1
	v_ashrrev_i32_e32 v1, 5, v1
	v_add_u32_e32 v12, v1, v2
	v_ashrrev_i32_e32 v13, 31, v12
	v_lshlrev_b64 v[2:3], 3, v[12:13]
	s_waitcnt lgkmcnt(0)
	v_lshl_add_u64 v[4:5], s[6:7], 0, v[2:3]
	global_load_dwordx2 v[4:5], v[4:5], off
	s_movk_i32 s0, 0xff40
	v_mad_u64_u32 v[0:1], s[0:1], v12, s0, v[0:1]
	s_movk_i32 s2, 0xc00
	v_add_u32_e32 v8, 0x1800, v12
	v_mov_b64_e32 v[6:7], s[4:5]
	v_ashrrev_i32_e32 v1, 31, v0
	v_mad_i64_i32 v[8:9], s[0:1], v8, s2, v[6:7]
	v_lshlrev_b64 v[14:15], 4, v[0:1]
	v_lshl_add_u64 v[2:3], s[8:9], 0, v[2:3]
	v_lshl_add_u64 v[8:9], v[8:9], 0, v[14:15]
	global_load_dwordx2 v[16:17], v[2:3], off
	s_waitcnt vmcnt(1)
	v_mad_i64_i32 v[0:1], s[0:1], v4, s2, v[6:7]
	v_mad_i64_i32 v[10:11], s[0:1], v5, s2, v[6:7]
	v_lshl_add_u64 v[18:19], v[0:1], 0, v[14:15]
	global_load_dwordx4 v[0:3], v[8:9], off
	global_load_dwordx4 v[4:7], v[18:19], off
	v_lshl_add_u64 v[8:9], v[10:11], 0, v[14:15]
	global_load_dwordx4 v[8:11], v[8:9], off
	v_mov_b64_e32 v[18:19], s[10:11]
	v_mad_i64_i32 v[12:13], s[0:1], v12, s2, v[18:19]
	v_lshl_add_u64 v[12:13], v[12:13], 0, v[14:15]
	s_waitcnt vmcnt(1)
	v_pk_fma_f32 v[0:1], v[16:17], v[4:5], v[0:1] op_sel_hi:[0,1,1]
	v_pk_fma_f32 v[2:3], v[16:17], v[6:7], v[2:3] op_sel_hi:[0,1,1]
	s_waitcnt vmcnt(0)
	v_pk_fma_f32 v[0:1], v[16:17], v[8:9], v[0:1] op_sel:[1,0,0]
	v_pk_fma_f32 v[2:3], v[16:17], v[10:11], v[2:3] op_sel:[1,0,0]
	global_store_dwordx4 v[12:13], v[0:3], off
	s_endpgm
	s_nop 0
	s_nop 0
	s_nop 0
	s_nop 0
	s_nop 0
	s_nop 0
	s_nop 0
	s_nop 0
	s_nop 0
	s_nop 0
	s_nop 0
	s_nop 0
	s_nop 0
	s_nop 0
	s_nop 0
	s_nop 0
	s_nop 0
	s_nop 0
	s_nop 0
	s_nop 0
	s_nop 0
	s_nop 0
	s_nop 0
	s_nop 0
	s_nop 0
	s_nop 0
	s_nop 0
	s_nop 0
	s_nop 0
	s_nop 0
	s_nop 0
	s_nop 0
	s_nop 0
	s_nop 0
	s_nop 0
	s_nop 0
	s_nop 0
	s_nop 0
	s_nop 0
	s_nop 0
	s_nop 0
	s_nop 0
	s_nop 0
	s_nop 0
	s_nop 0
	s_nop 0
	s_nop 0
	s_nop 0
	s_endpgm

_Z11gemm_kernelILi128ELi192ELi1EEv8GemmArgs:
	s_load_dwordx2 s[4:5], s[0:1], 0x38
	s_addk_i32 s2, 0xe0
	s_mov_b32 s3, 0
	s_lshl_b64 s[6:7], s[2:3], 2
	s_waitcnt lgkmcnt(0)
	s_add_u32 s4, s4, s6
	s_addc_u32 s5, s5, s7
	s_load_dword s8, s[4:5], 0x0
	s_waitcnt lgkmcnt(0)
	s_cmp_lt_i32 s8, 0
	s_cbranch_scc1 .LBB3_4
	s_load_dwordx2 s[6:7], s[0:1], 0x48
	s_load_dwordx2 s[4:5], s[0:1], 0x0
	v_lshlrev_b32_e32 v64, 4, v0
	v_and_b32_e32 v1, 32, v0
	v_bitop3_b32 v1, v64, v1, 48 bitop3:0x6c
	s_and_b32 s2, s8, 0xffff
	v_bfe_u32 v4, v0, 2, 4
	v_lshrrev_b32_e32 v2, 1, v0
	v_lshrrev_b32_e32 v1, 1, v1
	v_lshrrev_b32_e32 v6, 3, v0
	v_and_or_b32 v1, v2, 32, v1
	v_add_u32_e32 v5, s2, v4
	v_and_b32_e32 v7, 48, v6
	s_movk_i32 s10, 0x70
	v_add_lshl_u32 v22, v5, v7, 12
	v_mov_b32_e32 v23, 0
	v_lshlrev_b32_e32 v44, 1, v1
	v_bitop3_b32 v1, v6, s10, 64 bitop3:0xc8
	s_waitcnt lgkmcnt(0)
	v_lshl_add_u64 v[2:3], s[4:5], 0, v[22:23]
	v_mov_b32_e32 v45, v23
	v_add_lshl_u32 v48, v5, v1, 12
	v_mov_b32_e32 v49, v23
	s_lshr_b32 s10, s8, 24
	s_bfe_u32 s9, s8, 0x80010
	v_lshl_add_u64 v[46:47], v[2:3], 0, v[44:45]
	v_lshl_add_u64 v[2:3], s[4:5], 0, v[48:49]
	s_mulk_i32 s10, 0x300
	v_lshl_add_u64 v[50:51], v[2:3], 0, v[44:45]
	s_mul_i32 s8, s9, 0xc0
	v_or_b32_e32 v2, s10, v4
	v_add_u32_e32 v4, s8, v2
	v_or_b32_e32 v2, v4, v7
	v_lshlrev_b32_e32 v52, 12, v2
	v_mov_b32_e32 v53, v23
	v_lshl_add_u64 v[2:3], s[6:7], 0, v[52:53]
	v_add_lshl_u32 v56, v4, v1, 12
	v_mov_b32_e32 v57, v23
	v_lshl_add_u64 v[54:55], v[2:3], 0, v[44:45]
	v_lshl_add_u64 v[2:3], s[6:7], 0, v[56:57]
	v_add_u32_e32 v60, 0x80000, v52
	v_mov_b32_e32 v61, v23
	v_lshl_add_u64 v[58:59], v[2:3], 0, v[44:45]
	v_lshl_add_u64 v[2:3], s[6:7], 0, v[60:61]
	v_lshl_add_u64 v[62:63], v[2:3], 0, v[44:45]
	v_readfirstlane_b32 s16, v0
	s_load_dwordx2 s[0:1], s[0:1], 0x98
	s_lshr_b32 s16, s16, 6
	s_lshl_b32 s16, s16, 10
	v_bfe_u32 v1, v0, 6, 2
	v_lshrrev_b32_e32 v80, 2, v0
	s_add_u32 m0, s16, 0
	s_nop 0
	global_load_lds_dwordx4 v[46:47], off
	s_add_u32 m0, s16, 8192
	s_nop 0
	global_load_lds_dwordx4 v[50:51], off
	s_add_u32 m0, s16, 16384
	s_nop 0
	global_load_lds_dwordx4 v[54:55], off
	s_add_u32 m0, s16, 24576
	s_nop 0
	global_load_lds_dwordx4 v[58:59], off
	s_add_u32 m0, s16, 32768
	s_nop 0
	global_load_lds_dwordx4 v[62:63], off
	s_add_u32 m0, s16, 40832
	s_nop 0
	global_load_lds_dwordx4 v[46:47], off offset:128
	s_add_u32 m0, s16, 49024
	s_nop 0
	global_load_lds_dwordx4 v[50:51], off offset:128
	s_add_u32 m0, s16, 57216
	s_nop 0
	global_load_lds_dwordx4 v[54:55], off offset:128
	s_add_u32 m0, s16, 65408
	s_nop 0
	global_load_lds_dwordx4 v[58:59], off offset:128
	s_add_u32 m0, s16, 73600
	s_nop 0
	global_load_lds_dwordx4 v[62:63], off offset:128
	s_mov_b32 s17, 0
	s_mov_b32 s18, 0xa000
	s_mov_b32 s19, 0x14000
	v_lshlrev_b32_e32 v25, 6, v0
	v_lshlrev_b32_e32 v27, 2, v0
	v_and_b32_e32 v24, 48, v0
	v_and_b32_e32 v25, 0x3c0, v25
	v_and_b32_e32 v27, 32, v27
	v_or_b32_e32 v26, v25, v24
	v_bitop3_b32 v87, v25, v27, v24 bitop3:0x36
	v_or_b32_e32 v24, v44, v60
	v_mov_b32_e32 v25, v23
	v_lshl_add_u64 v[24:25], s[6:7], 0, v[24:25]
	s_mov_b64 s[10:11], 0x100
	v_lshl_add_u64 v[70:71], v[24:25], 0, s[10:11]
	v_or_b32_e32 v24, v56, v44
	v_mov_b32_e32 v25, v23
	v_lshl_add_u64 v[24:25], s[6:7], 0, v[24:25]
	v_lshl_add_u64 v[72:73], v[24:25], 0, s[10:11]
	v_or_b32_e32 v24, v52, v44
	v_mov_b32_e32 v25, v23
	v_lshl_add_u64 v[24:25], s[6:7], 0, v[24:25]
	v_lshl_add_u64 v[74:75], v[24:25], 0, s[10:11]
	v_or_b32_e32 v24, v48, v44
	v_mov_b32_e32 v25, v23
	v_lshl_add_u64 v[24:25], s[4:5], 0, v[24:25]
	v_or_b32_e32 v22, v22, v44
	v_and_b32_e32 v81, 64, v80
	v_mul_u32_u24_e32 v86, 0x1800, v1
	v_lshl_add_u64 v[76:77], v[24:25], 0, s[10:11]
	v_lshl_add_u64 v[24:25], s[4:5], 0, v[22:23]
	v_bitop3_b32 v82, v26, v86, v27 bitop3:0xde
	v_lshlrev_b32_e32 v88, 7, v81
	v_lshl_add_u64 v[78:79], v[24:25], 0, s[10:11]
	s_mov_b64 s[4:5], 0
	v_mov_b32_e32 v22, v23
	v_mov_b32_e32 v24, v23
	v_mov_b32_e32 v25, v23
	v_mov_b32_e32 v50, v23
	v_mov_b32_e32 v51, v23
	v_mov_b32_e32 v52, v23
	v_mov_b32_e32 v54, v23
	v_mov_b32_e32 v55, v23
	v_mov_b32_e32 v56, v23
	v_mov_b32_e32 v58, v23
	v_mov_b32_e32 v59, v23
	v_mov_b32_e32 v60, v23
	v_mov_b32_e32 v66, v23
	v_mov_b32_e32 v67, v23
	v_mov_b32_e32 v68, v23
	v_mov_b32_e32 v69, v23
	v_mov_b32_e32 v62, v23
	v_mov_b32_e32 v63, v23
	v_mov_b32_e32 v64, v23
	v_mov_b32_e32 v65, v23
	v_mov_b32_e32 v42, v23
	v_mov_b32_e32 v43, v23
	v_mov_b32_e32 v44, v23
	v_mov_b32_e32 v46, v23
	v_mov_b32_e32 v47, v23
	v_mov_b32_e32 v48, v23
	v_mov_b32_e32 v30, v23
	v_mov_b32_e32 v31, v23
	v_mov_b32_e32 v32, v23
	v_mov_b32_e32 v33, v23
	v_mov_b32_e32 v34, v23
	v_mov_b32_e32 v35, v23
	v_mov_b32_e32 v36, v23
	v_mov_b32_e32 v37, v23
	v_mov_b32_e32 v38, v23
	v_mov_b32_e32 v39, v23
	v_mov_b32_e32 v40, v23
	v_mov_b32_e32 v41, v23
	v_mov_b32_e32 v26, v23
	v_mov_b32_e32 v27, v23
	v_mov_b32_e32 v28, v23
	v_mov_b32_e32 v29, v23
	s_waitcnt vmcnt(5) lgkmcnt(0)
	s_barrier
.Ldn_loop:
	s_mov_b32 s7, s17
	v_or_b32_e32 v89, s7, v87
	v_add_u32_e32 v122, v89, v88
	ds_read_b128 v[90:93], v122
	ds_read_b128 v[94:97], v122 offset:2048
	ds_read_b128 v[98:101], v122 offset:4096
	ds_read_b128 v[102:105], v122 offset:6144
	v_add_u32_e32 v89, v89, v86
	ds_read_b128 v[106:109], v89 offset:16384
	ds_read_b128 v[110:113], v89 offset:18432
	ds_read_b128 v[114:117], v89 offset:20480
	s_add_u32 s6, s19, s16
	s_mov_b32 m0, s6
	v_lshl_add_u64 v[2:3], v[78:79], 0, s[4:5]
	global_load_lds_dwordx4 v[2:3], off
	s_waitcnt lgkmcnt(2)
	v_mfma_f32_16x16x32_f16 v[22:25], v[90:93], v[106:109], v[22:25]
	s_waitcnt lgkmcnt(1)
	v_mfma_f32_16x16x32_f16 v[50:53], v[90:93], v[110:113], v[50:53]
	s_waitcnt lgkmcnt(0)
	v_mfma_f32_16x16x32_f16 v[54:57], v[90:93], v[114:117], v[54:57]
	s_add_u32 m0, s6, 8192
	v_lshl_add_u64 v[4:5], v[76:77], 0, s[4:5]
	global_load_lds_dwordx4 v[4:5], off
	v_mfma_f32_16x16x32_f16 v[58:61], v[94:97], v[106:109], v[58:61]
	v_mfma_f32_16x16x32_f16 v[66:69], v[94:97], v[110:113], v[66:69]
	v_mfma_f32_16x16x32_f16 v[62:65], v[94:97], v[114:117], v[62:65]
	ds_read_b128 v[90:93], v122 offset:1024
	ds_read_b128 v[94:97], v122 offset:3072
	ds_read_b128 v[118:121], v122 offset:5120
	ds_read_b128 v[122:125], v122 offset:7168
	v_add_u32_e32 v134, s7, v82
	ds_read_b128 v[126:129], v134 offset:17408
	ds_read_b128 v[130:133], v134 offset:19456
	ds_read_b128 v[134:137], v134 offset:21504
	s_add_u32 m0, s6, 16384
	v_lshl_add_u64 v[6:7], v[74:75], 0, s[4:5]
	global_load_lds_dwordx4 v[6:7], off
	v_mfma_f32_16x16x32_f16 v[42:45], v[98:101], v[106:109], v[42:45]
	v_mfma_f32_16x16x32_f16 v[46:49], v[98:101], v[110:113], v[46:49]
	v_mfma_f32_16x16x32_f16 v[30:33], v[98:101], v[114:117], v[30:33]
	s_add_u32 m0, s6, 24576
	v_lshl_add_u64 v[8:9], v[72:73], 0, s[4:5]
	global_load_lds_dwordx4 v[8:9], off
	v_mfma_f32_16x16x32_f16 v[34:37], v[102:105], v[106:109], v[34:37]
	v_mfma_f32_16x16x32_f16 v[38:41], v[102:105], v[110:113], v[38:41]
	v_mfma_f32_16x16x32_f16 v[26:29], v[102:105], v[114:117], v[26:29]
	s_add_u32 m0, s6, 32768
	v_lshl_add_u64 v[10:11], v[70:71], 0, s[4:5]
	global_load_lds_dwordx4 v[10:11], off
	s_waitcnt lgkmcnt(2)
	v_mfma_f32_16x16x32_f16 v[22:25], v[90:93], v[126:129], v[22:25]
	s_waitcnt lgkmcnt(1)
	v_mfma_f32_16x16x32_f16 v[50:53], v[90:93], v[130:133], v[50:53]
	s_waitcnt lgkmcnt(0)
	v_mfma_f32_16x16x32_f16 v[54:57], v[90:93], v[134:137], v[54:57]
	v_mfma_f32_16x16x32_f16 v[58:61], v[94:97], v[126:129], v[58:61]
	v_mfma_f32_16x16x32_f16 v[66:69], v[94:97], v[130:133], v[66:69]
	v_mfma_f32_16x16x32_f16 v[62:65], v[94:97], v[134:137], v[62:65]
	v_mfma_f32_16x16x32_f16 v[42:45], v[118:121], v[126:129], v[42:45]
	v_mfma_f32_16x16x32_f16 v[46:49], v[118:121], v[130:133], v[46:49]
	v_mfma_f32_16x16x32_f16 v[30:33], v[118:121], v[134:137], v[30:33]
	v_mfma_f32_16x16x32_f16 v[34:37], v[122:125], v[126:129], v[34:37]
	v_mfma_f32_16x16x32_f16 v[38:41], v[122:125], v[130:133], v[38:41]
	v_mfma_f32_16x16x32_f16 v[26:29], v[122:125], v[134:137], v[26:29]
	s_add_i32 s3, s3, 1
	s_add_u32 s4, s4, 0x80
	s_addc_u32 s5, s5, 0
	s_cmpk_eq_i32 s4, 0xf00
	s_waitcnt vmcnt(5) lgkmcnt(0)
	s_barrier
	s_mov_b32 s20, s17
	s_mov_b32 s17, s18
	s_mov_b32 s18, s19
	s_mov_b32 s19, s20
	s_cbranch_scc0 .Ldn_loop
	v_add_u32_e32 v78, v87, v88
	ds_read_b128 v[70:73], v78 offset:2048
	ds_read_b128 v[74:77], v78 offset:4096
	ds_read_b128 v[86:89], v78 offset:6144
	ds_read_b128 v[90:93], v82 offset:16384
	ds_read_b128 v[94:97], v82 offset:18432
	ds_read_b128 v[98:101], v78
	ds_read_b128 v[102:105], v82 offset:20480
	s_waitcnt lgkmcnt(1)
	v_mfma_f32_16x16x32_f16 v[22:25], v[98:101], v[90:93], v[22:25]
	v_mfma_f32_16x16x32_f16 v[50:53], v[98:101], v[94:97], v[50:53]
	s_waitcnt lgkmcnt(0)
	v_mfma_f32_16x16x32_f16 v[18:21], v[98:101], v[102:105], v[54:57]
	v_mfma_f32_16x16x32_f16 v[54:57], v[70:73], v[90:93], v[58:61]
	v_mfma_f32_16x16x32_f16 v[58:61], v[70:73], v[94:97], v[66:69]
	v_mfma_f32_16x16x32_f16 v[14:17], v[70:73], v[102:105], v[62:65]
	s_nop 2
	ds_read_b128 v[62:65], v78 offset:3072
	ds_read_b128 v[66:69], v78 offset:5120
	ds_read_b128 v[70:73], v78 offset:7168
	ds_read_b128 v[98:101], v82 offset:17408
	ds_read_b128 v[106:109], v82 offset:19456
	ds_read_b128 v[110:113], v78 offset:1024
	ds_read_b128 v[114:117], v82 offset:21504
	v_mfma_f32_16x16x32_f16 v[42:45], v[74:77], v[90:93], v[42:45]
	s_mov_b32 s3, 0xe000
	v_mfma_f32_16x16x32_f16 v[46:49], v[74:77], v[94:97], v[46:49]
	v_mfma_f32_16x16x32_f16 v[10:13], v[74:77], v[102:105], v[30:33]
	v_mfma_f32_16x16x32_f16 v[30:33], v[86:89], v[90:93], v[34:37]
	v_mfma_f32_16x16x32_f16 v[34:37], v[86:89], v[94:97], v[38:41]
	v_mfma_f32_16x16x32_f16 v[6:9], v[86:89], v[102:105], v[26:29]
	s_waitcnt lgkmcnt(1)
	v_mfma_f32_16x16x32_f16 v[22:25], v[110:113], v[98:101], v[22:25]
	v_mfma_f32_16x16x32_f16 v[26:29], v[110:113], v[106:109], v[50:53]
	s_waitcnt lgkmcnt(0)
	v_mfma_f32_16x16x32_f16 v[2:5], v[110:113], v[114:117], v[18:21]
	v_mfma_f32_16x16x32_f16 v[18:21], v[62:65], v[98:101], v[54:57]
	v_mfma_f32_16x16x32_f16 v[38:41], v[62:65], v[106:109], v[58:61]
	v_mfma_f32_16x16x32_f16 v[14:17], v[62:65], v[114:117], v[14:17]
	v_mfma_f32_16x16x32_f16 v[42:45], v[66:69], v[98:101], v[42:45]
	v_mfma_f32_16x16x32_f16 v[46:49], v[66:69], v[106:109], v[46:49]
	v_mfma_f32_16x16x32_f16 v[10:13], v[66:69], v[114:117], v[10:13]
	v_mfma_f32_16x16x32_f16 v[30:33], v[70:73], v[98:101], v[30:33]
	v_mfma_f32_16x16x32_f16 v[34:37], v[70:73], v[106:109], v[34:37]
	v_mfma_f32_16x16x32_f16 v[6:9], v[70:73], v[114:117], v[6:9]
	s_waitcnt vmcnt(0) lgkmcnt(0)
	s_barrier
	ds_read_b128 v[50:53], v78 offset:43008
	ds_read_b128 v[54:57], v78 offset:45056
	ds_read_b128 v[58:61], v78 offset:47104
	ds_read_b128 v[62:65], v82 offset:57344
	ds_read_b128 v[66:69], v82 offset:59392
	ds_read_b128 v[70:73], v78 offset:40960
	ds_read_b128 v[74:77], v82 offset:61440
	s_waitcnt lgkmcnt(1)
	v_mfma_f32_16x16x32_f16 v[22:25], v[70:73], v[62:65], v[22:25]
	v_mfma_f32_16x16x32_f16 v[26:29], v[70:73], v[66:69], v[26:29]
	s_waitcnt lgkmcnt(0)
	v_mfma_f32_16x16x32_f16 v[2:5], v[70:73], v[74:77], v[2:5]
	v_mfma_f32_16x16x32_f16 v[18:21], v[50:53], v[62:65], v[18:21]
	v_mfma_f32_16x16x32_f16 v[38:41], v[50:53], v[66:69], v[38:41]
	v_mfma_f32_16x16x32_f16 v[14:17], v[50:53], v[74:77], v[14:17]
	ds_read_b128 v[50:53], v78 offset:44032
	ds_read_b128 v[70:73], v78 offset:46080
	ds_read_b128 v[84:87], v78 offset:48128
	ds_read_b128 v[88:91], v82 offset:58368
	ds_read_b128 v[92:95], v82 offset:60416
	ds_read_b128 v[96:99], v78 offset:41984
	ds_read_b128 v[100:103], v82 offset:62464
	v_mfma_f32_16x16x32_f16 v[42:45], v[54:57], v[62:65], v[42:45]
	v_mfma_f32_16x16x32_f16 v[46:49], v[54:57], v[66:69], v[46:49]
	v_mfma_f32_16x16x32_f16 v[10:13], v[54:57], v[74:77], v[10:13]
	v_mfma_f32_16x16x32_f16 v[30:33], v[58:61], v[62:65], v[30:33]
	v_mfma_f32_16x16x32_f16 v[34:37], v[58:61], v[66:69], v[34:37]
	v_mfma_f32_16x16x32_f16 v[6:9], v[58:61], v[74:77], v[6:9]
	s_waitcnt lgkmcnt(1)
	v_mfma_f32_16x16x32_f16 v[22:25], v[96:99], v[88:91], v[22:25]
	v_mfma_f32_16x16x32_f16 v[26:29], v[96:99], v[92:95], v[26:29]
	s_waitcnt lgkmcnt(0)
	v_mfma_f32_16x16x32_f16 v[2:5], v[96:99], v[100:103], v[2:5]
	v_mfma_f32_16x16x32_f16 v[18:21], v[50:53], v[88:91], v[18:21]
	v_mfma_f32_16x16x32_f16 v[38:41], v[50:53], v[92:95], v[38:41]
	v_mfma_f32_16x16x32_f16 v[14:17], v[50:53], v[100:103], v[14:17]
	v_mfma_f32_16x16x32_f16 v[42:45], v[70:73], v[88:91], v[42:45]
	v_mfma_f32_16x16x32_f16 v[46:49], v[70:73], v[92:95], v[46:49]
	v_mfma_f32_16x16x32_f16 v[10:13], v[70:73], v[100:103], v[10:13]
	v_mfma_f32_16x16x32_f16 v[30:33], v[84:87], v[88:91], v[30:33]
	v_mfma_f32_16x16x32_f16 v[34:37], v[84:87], v[92:95], v[34:37]
	v_mfma_f32_16x16x32_f16 v[6:9], v[84:87], v[100:103], v[6:9]
	v_and_or_b32 v50, v80, 12, v81
	v_add_u32_e32 v50, s2, v50
	v_mul_u32_u24_e32 v1, 48, v1
	v_and_or_b32 v52, v0, 15, v1
	v_mul_u32_u24_e32 v0, 0xc00, v50
	v_mov_b32_e32 v1, 0
	v_lshl_add_u64 v[50:51], s[0:1], 0, v[0:1]
	v_add_lshl_u32 v0, v52, s8, 2
	v_lshl_add_u64 v[0:1], v[50:51], 0, v[0:1]
	s_mov_b64 s[0:1], 0x1800
	s_barrier
	global_store_dword v[0:1], v22, off
	global_store_dword v[0:1], v26, off offset:64
	global_store_dword v[0:1], v2, off offset:128
	global_store_dword v[0:1], v23, off offset:3072
	global_store_dword v[0:1], v27, off offset:3136
	global_store_dword v[0:1], v3, off offset:3200
	v_lshl_add_u64 v[2:3], v[0:1], 0, s[0:1]
	s_movk_i32 s0, 0x1000
	v_add_co_u32_e32 v22, vcc, s0, v0
	s_mov_b64 s[0:1], 0x2400
	s_nop 0
	v_addc_co_u32_e32 v23, vcc, 0, v1, vcc
	global_store_dword v[22:23], v24, off offset:2048
	global_store_dword v[2:3], v28, off offset:64
	global_store_dword v[2:3], v4, off offset:128
	v_lshl_add_u64 v[2:3], v[0:1], 0, s[0:1]
	s_movk_i32 s0, 0x2000
	v_add_co_u32_e32 v22, vcc, s0, v0
	s_mov_b64 s[0:1], 0xc000
	s_nop 0
	v_addc_co_u32_e32 v23, vcc, 0, v1, vcc
	global_store_dword v[22:23], v25, off offset:1024
	global_store_dword v[2:3], v29, off offset:64
	global_store_dword v[2:3], v5, off offset:128
	v_lshl_add_u64 v[2:3], v[0:1], 0, s[0:1]
	s_mov_b32 s0, 0xc000
	v_add_co_u32_e32 v4, vcc, s0, v0
	s_mov_b64 s[0:1], 0xcc00
	s_nop 0
	v_addc_co_u32_e32 v5, vcc, 0, v1, vcc
	global_store_dword v[4:5], v18, off
	global_store_dword v[2:3], v38, off offset:64
	global_store_dword v[2:3], v14, off offset:128
	v_lshl_add_u64 v[2:3], v[0:1], 0, s[0:1]
	s_mov_b64 s[0:1], 0xd800
	global_store_dword v[4:5], v19, off offset:3072
	global_store_dword v[2:3], v39, off offset:64
	global_store_dword v[2:3], v15, off offset:128
	v_lshl_add_u64 v[2:3], v[0:1], 0, s[0:1]
	s_mov_b32 s0, 0xd000
	v_add_co_u32_e32 v4, vcc, s0, v0
	s_mov_b64 s[0:1], 0xe400
	s_nop 0
	v_addc_co_u32_e32 v5, vcc, 0, v1, vcc
	global_store_dword v[4:5], v20, off offset:2048
	global_store_dword v[2:3], v40, off offset:64
	global_store_dword v[2:3], v16, off offset:128
	v_add_co_u32_e32 v4, vcc, s3, v0
	v_lshl_add_u64 v[2:3], v[0:1], 0, s[0:1]
	s_nop 0
	v_addc_co_u32_e32 v5, vcc, 0, v1, vcc
	s_mov_b64 s[0:1], 0x18000
	global_store_dword v[4:5], v21, off offset:1024
	global_store_dword v[2:3], v41, off offset:64
	global_store_dword v[2:3], v17, off offset:128
	v_lshl_add_u64 v[2:3], v[0:1], 0, s[0:1]
	s_mov_b32 s0, 0x18000
	v_add_co_u32_e32 v4, vcc, s0, v0
	s_mov_b64 s[0:1], 0x18c00
	s_nop 0
	v_addc_co_u32_e32 v5, vcc, 0, v1, vcc
	global_store_dword v[4:5], v42, off
	global_store_dword v[2:3], v46, off offset:64
	global_store_dword v[2:3], v10, off offset:128
	v_lshl_add_u64 v[2:3], v[0:1], 0, s[0:1]
	s_mov_b64 s[0:1], 0x19800
	global_store_dword v[4:5], v43, off offset:3072
	global_store_dword v[2:3], v47, off offset:64
	global_store_dword v[2:3], v11, off offset:128
	v_lshl_add_u64 v[2:3], v[0:1], 0, s[0:1]
	s_mov_b32 s0, 0x19000
	v_add_co_u32_e32 v4, vcc, s0, v0
	s_mov_b64 s[0:1], 0x1a400
	s_nop 0
	v_addc_co_u32_e32 v5, vcc, 0, v1, vcc
	global_store_dword v[4:5], v44, off offset:2048
	global_store_dword v[2:3], v48, off offset:64
	global_store_dword v[2:3], v12, off offset:128
	v_lshl_add_u64 v[2:3], v[0:1], 0, s[0:1]
	s_mov_b32 s0, 0x1a000
	v_add_co_u32_e32 v4, vcc, s0, v0
	s_mov_b64 s[0:1], 0x24000
	s_nop 0
	v_addc_co_u32_e32 v5, vcc, 0, v1, vcc
	global_store_dword v[4:5], v45, off offset:1024
	global_store_dword v[2:3], v49, off offset:64
	global_store_dword v[2:3], v13, off offset:128
	v_lshl_add_u64 v[2:3], v[0:1], 0, s[0:1]
	s_mov_b32 s0, 0x24000
	v_add_co_u32_e32 v4, vcc, s0, v0
	s_mov_b64 s[0:1], 0x24c00
	s_nop 0
	v_addc_co_u32_e32 v5, vcc, 0, v1, vcc
	global_store_dword v[4:5], v30, off
	global_store_dword v[2:3], v34, off offset:64
	global_store_dword v[2:3], v6, off offset:128
	v_lshl_add_u64 v[2:3], v[0:1], 0, s[0:1]
	s_mov_b64 s[0:1], 0x25800
	global_store_dword v[4:5], v31, off offset:3072
	global_store_dword v[2:3], v35, off offset:64
	global_store_dword v[2:3], v7, off offset:128
	v_lshl_add_u64 v[2:3], v[0:1], 0, s[0:1]
	s_mov_b32 s0, 0x25000
	v_add_co_u32_e32 v4, vcc, s0, v0
	s_mov_b64 s[0:1], 0x26400
	s_nop 0
	v_addc_co_u32_e32 v5, vcc, 0, v1, vcc
	global_store_dword v[4:5], v32, off offset:2048
	global_store_dword v[2:3], v36, off offset:64
	global_store_dword v[2:3], v8, off offset:128
	v_lshl_add_u64 v[2:3], v[0:1], 0, s[0:1]
	v_add_co_u32_e32 v0, vcc, 0x26000, v0
	s_nop 1
	v_addc_co_u32_e32 v1, vcc, 0, v1, vcc
	global_store_dword v[0:1], v33, off offset:1024
	global_store_dword v[2:3], v37, off offset:64
	global_store_dword v[2:3], v9, off offset:128

	.amdhsa_kernel _Z11gemm_kernelILi128ELi192ELi1EEv8GemmArgs
		.amdhsa_group_segment_fixed_size 122880
		.amdhsa_private_segment_fixed_size 0
		.amdhsa_kernarg_size 160
		.amdhsa_user_sgpr_count 2
		.amdhsa_user_sgpr_dispatch_ptr 0
		.amdhsa_user_sgpr_queue_ptr 0
		.amdhsa_user_sgpr_kernarg_segment_ptr 1
		.amdhsa_user_sgpr_dispatch_id 0
		.amdhsa_user_sgpr_kernarg_preload_length 0
		.amdhsa_user_sgpr_kernarg_preload_offset 0
		.amdhsa_user_sgpr_private_segment_size 0
		.amdhsa_uses_dynamic_stack 0
		.amdhsa_enable_private_segment 0
		.amdhsa_system_sgpr_workgroup_id_x 1
		.amdhsa_system_sgpr_workgroup_id_y 0
		.amdhsa_system_sgpr_workgroup_id_z 0
		.amdhsa_system_sgpr_workgroup_info 0
		.amdhsa_system_vgpr_workitem_id 0
		.amdhsa_next_free_vgpr 138
		.amdhsa_next_free_sgpr 96
		.amdhsa_accum_offset 140
		.amdhsa_reserve_vcc 1
		.amdhsa_float_round_mode_32 0
		.amdhsa_float_round_mode_16_64 0
		.amdhsa_float_denorm_mode_32 3
		.amdhsa_float_denorm_mode_16_64 3
		.amdhsa_dx10_clamp 1
		.amdhsa_ieee_mode 1
		.amdhsa_fp16_overflow 0
		.amdhsa_tg_split 0
		.amdhsa_exception_fp_ieee_invalid_op 0
		.amdhsa_exception_fp_denorm_src 0
		.amdhsa_exception_fp_ieee_div_zero 0
		.amdhsa_exception_fp_ieee_overflow 0
		.amdhsa_exception_fp_ieee_underflow 0
		.amdhsa_exception_fp_ieee_inexact 0
		.amdhsa_exception_int_div_zero 0
	.end_amdhsa_kernel

amdhsa.kernels:
  - .agpr_count:     0
    .args:
      - .actual_access:  read_only
        .address_space:  global
        .offset:         0
        .size:           8
        .value_kind:     global_buffer
      - .actual_access:  read_only
        .address_space:  global
        .offset:         8
        .size:           8
        .value_kind:     global_buffer
      - .actual_access:  write_only
        .address_space:  global
        .offset:         16
        .size:           8
        .value_kind:     global_buffer
      - .actual_access:  write_only
        .address_space:  global
        .offset:         24
        .size:           8
        .value_kind:     global_buffer
      - .actual_access:  write_only
        .address_space:  global
        .offset:         32
        .size:           8
        .value_kind:     global_buffer
      - .actual_access:  read_only
        .address_space:  global
        .offset:         40
        .size:           8
        .value_kind:     global_buffer
    .group_segment_fixed_size: 0
    .kernarg_segment_align: 8
    .kernarg_segment_size: 48
    .language:       OpenCL C
    .language_version:
      - 2
      - 0
    .max_flat_workgroup_size: 256
    .name:           _Z11gate_kernelPKfS0_PDF16_PiPfS3_
    .private_segment_fixed_size: 0
    .sgpr_count:     26
    .sgpr_spill_count: 0
    .symbol:         _Z11gate_kernelPKfS0_PDF16_PiPfS3_.kd
    .uniform_work_group_size: 1
    .uses_dynamic_stack: false
    .vgpr_count:     113
    .vgpr_spill_count: 0
    .wavefront_size: 64
  - .agpr_count:     0
    .args:
      - .offset:         0
        .size:           160
        .value_kind:     by_value
    .group_segment_fixed_size: 149540
    .kernarg_segment_align: 8
    .kernarg_segment_size: 160
    .language:       OpenCL C
    .language_version:
      - 2
      - 0
    .max_flat_workgroup_size: 512
    .name:           _Z9up_kernel8GemmArgs
    .private_segment_fixed_size: 0
    .sgpr_count:     82
    .sgpr_spill_count: 0
    .symbol:         _Z9up_kernel8GemmArgs.kd
    .uniform_work_group_size: 1
    .uses_dynamic_stack: false
    .vgpr_count:     256
    .vgpr_spill_count: 0
    .wavefront_size: 64
  - .agpr_count:     0
    .args:
      - .actual_access:  read_only
        .address_space:  global
        .offset:         0
        .size:           8
        .value_kind:     global_buffer
      - .actual_access:  read_only
        .address_space:  global
        .offset:         8
        .size:           8
        .value_kind:     global_buffer
      - .actual_access:  read_only
        .address_space:  global
        .offset:         16
        .size:           8
        .value_kind:     global_buffer
      - .actual_access:  write_only
        .address_space:  global
        .offset:         24
        .size:           8
        .value_kind:     global_buffer
    .group_segment_fixed_size: 0
    .kernarg_segment_align: 8
    .kernarg_segment_size: 32
    .language:       OpenCL C
    .language_version:
      - 2
      - 0
    .max_flat_workgroup_size: 256
    .name:           _Z14combine_kernelPKfPKiS0_Pf
    .private_segment_fixed_size: 0
    .sgpr_count:     18
    .sgpr_spill_count: 0
    .symbol:         _Z14combine_kernelPKfPKiS0_Pf.kd
    .uniform_work_group_size: 1
    .uses_dynamic_stack: false
    .vgpr_count:     20
    .vgpr_spill_count: 0
    .wavefront_size: 64
  - .agpr_count:     0
    .args:
      - .offset:         0
        .size:           160
        .value_kind:     by_value
    .group_segment_fixed_size: 122880
    .kernarg_segment_align: 8
    .kernarg_segment_size: 160
    .language:       OpenCL C
    .language_version:
      - 2
      - 0
    .max_flat_workgroup_size: 512
    .name:           _Z11gemm_kernelILi128ELi192ELi1EEv8GemmArgs
    .private_segment_fixed_size: 0
    .sgpr_count:     18
    .sgpr_spill_count: 0
    .symbol:         _Z11gemm_kernelILi128ELi192ELi1EEv8GemmArgs.kd
    .uniform_work_group_size: 1
    .uses_dynamic_stack: false
    .vgpr_count:     138
    .vgpr_spill_count: 0
    .wavefront_size: 64
